# one-time start skew after the prologue: batch group g sleeps g x s_sleep 64 (~1.7 us) so the eight XCD groups' weight streams are de-phased; on top of the K-loop peel
# speedup vs baseline: 1.0061x; 1.0061x over previous
.LBB0_131:
	v_readlane_b32 s2, v254, 0
	s_ashr_i32 s2, s2, 31
	s_cmp_eq_u32 s40, 15
	v_writelane_b32 v254, s2, 10
	s_cselect_b64 s[2:3], -1, 0
	v_writelane_b32 v254, s2, 11
	s_cmp_eq_u32 s40, 14
	s_mov_b32 s27, 0
	v_writelane_b32 v254, s3, 12
	s_cselect_b64 s[2:3], -1, 0
	v_writelane_b32 v254, s2, 13
	s_cmp_eq_u32 s40, 13
	v_mbcnt_lo_u32_b32 v0, -1, 0
	v_writelane_b32 v254, s3, 14
	s_cselect_b64 s[2:3], -1, 0
	v_writelane_b32 v254, s2, 15
	s_cmp_eq_u32 s40, 12
	v_mov_b32_e32 v1, 0
	v_writelane_b32 v254, s3, 16
	s_cselect_b64 s[2:3], -1, 0
	v_writelane_b32 v254, s2, 17
	s_cmp_eq_u32 s40, 11
	v_mov_b32_e32 v230, 0x358637bd
	v_writelane_b32 v254, s3, 18
	s_cselect_b64 s[2:3], -1, 0
	v_writelane_b32 v254, s2, 19
	s_cmp_eq_u32 s40, 10
	v_mov_b32_e32 v231, 0x260
	v_writelane_b32 v254, s3, 20
	s_cselect_b64 s[2:3], -1, 0
	v_writelane_b32 v254, s2, 21
	s_cmp_eq_u32 s40, 9
	v_mov_b64_e32 v[202:203], 0x200
	v_writelane_b32 v254, s3, 22
	s_cselect_b64 s[2:3], -1, 0
	v_writelane_b32 v254, s2, 23
	s_cmp_eq_u32 s40, 8
	v_mov_b64_e32 v[204:205], 0x1ff
	v_writelane_b32 v254, s3, 24
	s_cselect_b64 s[2:3], -1, 0
	v_writelane_b32 v254, s2, 25
	s_cmp_eq_u32 s40, 7
	v_mbcnt_hi_u32_b32 v234, -1, v0
	v_writelane_b32 v254, s3, 26
	s_cselect_b64 s[2:3], -1, 0
	v_writelane_b32 v254, s2, 27
	s_cmp_eq_u32 s40, 6
	v_mov_b32_e32 v4, 0x3f803f80
	v_writelane_b32 v254, s3, 28
	s_cselect_b64 s[2:3], -1, 0
	v_writelane_b32 v254, s2, 29
	s_cmp_eq_u32 s40, 5
	v_mov_b32_e32 v239, 0x5000
	v_writelane_b32 v254, s3, 30
	s_cselect_b64 s[2:3], -1, 0
	v_writelane_b32 v254, s2, 31
	s_cmp_eq_u32 s40, 4
	v_mov_b32_e32 v240, 0x80
	v_writelane_b32 v254, s3, 32
	s_cselect_b64 s[2:3], -1, 0
	v_writelane_b32 v254, s2, 33
	s_cmp_eq_u32 s40, 3
	s_mov_b64 s[28:29], 0x80
	v_writelane_b32 v254, s3, 34
	s_cselect_b64 s[2:3], -1, 0
	v_writelane_b32 v254, s2, 35
	s_cmp_eq_u32 s40, 2
	s_nop 0
	v_writelane_b32 v254, s3, 36
	s_cselect_b64 s[2:3], -1, 0
	v_writelane_b32 v254, s2, 37
	s_cmp_eq_u32 s40, 1
	s_nop 0
	v_writelane_b32 v254, s3, 38
	s_cselect_b64 s[2:3], -1, 0
	v_writelane_b32 v254, s2, 39
	s_cmp_eq_u32 s40, 0
	s_nop 0
	v_writelane_b32 v254, s3, 40
	s_cselect_b64 s[2:3], -1, 0
	v_writelane_b32 v254, s2, 41
	s_lshl_b32 s4, s43, 14
	s_nop 0
	v_writelane_b32 v254, s3, 42
	s_lshl_b32 s2, s40, 6
	v_writelane_b32 v254, s2, 43
	v_writelane_b32 v254, s4, 44
	s_and_b32 s4, s33, 0x7c0
	v_writelane_b32 v254, s4, 45
	s_mulk_i32 s4, 0x1580
	s_lshl_b32 s2, s34, 3
	v_writelane_b32 v254, s4, 46
	s_and_b32 s2, s2, 0xfffff800
	s_and_b32 s3, s34, 0xff
	v_readlane_b32 s4, v254, 1
	s_cmp_lt_u32 s4, 8
	s_cselect_b64 s[4:5], -1, 0
	v_writelane_b32 v254, s4, 47
	s_or_b32 s2, s2, s3
	s_xor_b64 s[0:1], s[0:1], -1
	v_writelane_b32 v254, s5, 48
	v_writelane_b32 v254, s2, 49
	v_writelane_b32 v254, s0, 50
	s_mov_b32 s33, 0xf149f2ca
	s_mov_b32 s2, s27
	v_writelane_b32 v254, s1, 51
	s_add_i32 s0, 0, 0x20190
	v_writelane_b32 v254, s0, 52
	s_nop 0
	v_readlane_b32 s42, v254, 2
	v_readlane_b32 s43, v254, 3
	v_readlane_b32 s98, v254, 1
	s_nop 3
	s_and_b32 s98, s98, 7
	s_cmp_eq_u32 s98, 0
	s_cbranch_scc1 .Lskew_done
.Lskew_loop:
	s_sleep 64
	s_add_i32 s98, s98, -1
	s_cmp_lg_u32 s98, 0
	s_cbranch_scc1 .Lskew_loop
.Lskew_done:
	s_branch .LBB0_135
